# final_kernel: stacked address-math trim and single-op gather index guard on top of the fma fixed-point conversion
# baseline (speedup 1.0000x reference)
.LBB2_4:
	s_or_b64 exec, exec, s[4:5]
	s_load_dwordx2 s[26:27], s[0:1], 0x0
	v_lshlrev_b32_e32 v36, 3, v0
	s_and_saveexec_b64 s[4:5], s[2:3]
	v_mov_b32_e32 v4, 0
	v_mov_b32_e32 v5, v4
	ds_write_b64 v36, v[4:5]
	s_or_b64 exec, exec, s[4:5]
	s_load_dwordx2 s[24:25], s[0:1], 0x10
	v_cmp_eq_u32_e64 s[2:3], 0, v0
	s_and_saveexec_b64 s[4:5], s[2:3]
	v_mov_b32_e32 v4, 0
	ds_write_b32 v4, v4 offset:1568
	s_or_b64 exec, exec, s[4:5]
	v_mul_u32_u24_e32 v26, 0x1f40, v1
	v_mov_b32_e32 v27, 0
	v_max_i32_e32 v1, 1, v35
	v_and_b32_e32 v37, 3, v0
	v_add_u32_e32 v22, v26, v2
	v_add_u32_e32 v6, -1, v1
	v_lshlrev_b32_e32 v1, 1, v37
	v_cndmask_b32_e32 v22, 0, v22, vcc
	v_mov_b32_e32 v23, 0
	v_min_u32_e32 v2, v1, v6
	v_or_b32_e32 v30, 8, v1
	v_or_b32_e32 v25, 16, v1
	v_or_b32_e32 v24, 24, v1
	s_waitcnt lgkmcnt(0)
	v_lshl_add_u64 v[28:29], v[22:23], 3, s[26:27]
	v_add_lshl_u32 v2, v22, v2, 3
	v_min_u32_e32 v4, v30, v6
	v_add_lshl_u32 v4, v22, v4, 3
	global_load_dwordx4 v[14:17], v2, s[26:27]
	global_load_dwordx4 v[10:13], v4, s[26:27]
	v_min_u32_e32 v2, v25, v6
	v_min_u32_e32 v3, v24, v6
	v_add_lshl_u32 v2, v22, v2, 3
	v_add_lshl_u32 v3, v22, v3, 3
	global_load_dwordx4 v[6:9], v2, s[26:27]
	global_load_dwordx4 v[2:5], v3, s[26:27]
	v_cmp_lt_i32_e64 s[16:17], v1, v35
	v_mov_b32_e32 v26, 0
	s_and_saveexec_b64 s[2:3], s[16:17]
	s_cbranch_execz .LBB2_10
	s_waitcnt vmcnt(3)
	v_and_b32_e32 v26, 0x7ffff, v14
	v_min_u32_e32 v26, 0x7a11f, v26
	v_lshlrev_b32_e32 v26, 2, v26
	global_load_dword v26, v26, s[24:25]
	s_waitcnt vmcnt(0)
	v_mul_f32_e32 v26, v15, v26
